# k_gcn prologue first-index loads: plain loads + select instead of exec-masked loads
# baseline (speedup 1.0000x reference)
_Z5k_gcnILi128ELb1ELi16EEvPKDv8_DF16_PKiS4_PKfS2_S6_PDF16_S6_S6_S2_S6_S2_S6_S6_S6_PfS4_:
	s_load_dwordx4 s[20:23], s[0:1], 0x8
	s_load_dwordx2 s[4:5], s[0:1], 0x20
	v_readfirstlane_b32 s30, v0
	v_and_b32_e32 v1, 63, v0
	s_lshr_b32 s28, s30, 6
	v_lshl_or_b32 v2, s28, 9, v1
	v_mov_b32_e32 v3, 0
	v_bfe_u32 v83, v0, 4, 2
	s_waitcnt lgkmcnt(0)
	v_lshl_add_u64 v[14:15], v[2:3], 4, s[4:5]
	v_ashrrev_i32_e32 v3, 31, v2
	s_lshl_b32 s29, s2, 4
	v_lshl_add_u64 v[16:17], v[2:3], 4, s[4:5]
	global_load_dwordx4 v[26:29], v[14:15], off
	global_load_dwordx4 v[10:13], v[16:17], off offset:1024
	global_load_dwordx4 v[6:9], v[16:17], off offset:2048
	global_load_dwordx4 v[2:5], v[16:17], off offset:3072
	v_or_b32_e32 v14, s29, v83
	s_lshl_b32 s6, s28, 2
	v_add_u32_e32 v14, s6, v14
	s_movk_i32 s3, 0x1000
	v_ashrrev_i32_e32 v15, 31, v14
	v_add_co_u32_e32 v34, vcc, s3, v16
	v_lshl_add_u64 v[36:37], v[14:15], 2, s[20:21]
	s_nop 0
	v_addc_co_u32_e32 v35, vcc, 0, v17, vcc
	global_load_dwordx2 v[50:51], v[36:37], off
	global_load_dwordx4 v[30:33], v[34:35], off
	global_load_dwordx4 v[22:25], v[34:35], off offset:1024
	global_load_dwordx4 v[18:21], v[34:35], off offset:2048
	global_load_dwordx4 v[14:17], v[34:35], off offset:3072
	s_waitcnt vmcnt(4)
	v_sub_u32_e32 v53, v51, v50
	v_lshlrev_b32_e32 v34, 2, v50
	global_load_dword v36, v34, s[22:23]
	global_load_dword v38, v34, s[22:23] offset:4
	global_load_dword v42, v34, s[22:23] offset:8
	global_load_dword v46, v34, s[22:23] offset:12
	s_load_dwordx2 s[24:25], s[0:1], 0x0
	s_load_dwordx2 s[2:3], s[0:1], 0x18
	v_and_b32_e32 v82, 15, v0
	v_or_b32_e32 v51, s6, v83
	v_add_u32_e32 v34, s29, v51
	v_lshlrev_b32_e32 v54, 4, v82
	s_mov_b32 s27, 0x20000
	s_mov_b32 s26, 0x4e2100
	s_waitcnt lgkmcnt(0)
	s_and_b32 s25, s25, 0xffff
	v_lshl_or_b32 v35, v34, 8, v54
	buffer_load_dwordx4 v[64:67], v35, s[24:27], 0 offen
	v_ashrrev_i32_e32 v35, 31, v34
	v_lshl_add_u64 v[34:35], v[34:35], 2, s[2:3]
	global_load_dword v52, v[34:35], off
	v_mbcnt_lo_u32_b32 v34, -1, 0
	v_mbcnt_hi_u32_b32 v34, -1, v34
	v_and_b32_e32 v37, 64, v34
	v_xor_b32_e32 v35, 32, v34
	v_add_u32_e32 v37, 64, v37
	v_cmp_lt_i32_e32 vcc, v35, v37
	v_xor_b32_e32 v39, 16, v34
	s_load_dwordx2 s[2:3], s[0:1], 0x78
	s_load_dwordx8 s[4:11], s[0:1], 0x58
	s_load_dwordx8 s[12:19], s[0:1], 0x38
	v_cndmask_b32_e32 v35, v34, v35, vcc
	v_lshlrev_b32_e32 v84, 2, v35
	ds_bpermute_b32 v35, v84, v53
	v_cmp_lt_i32_e32 vcc, v39, v37
	s_mov_b32 s33, 4
	s_waitcnt vmcnt(1)
	v_mov_b32_e32 v70, 0x4e20
	v_cmp_lt_i32_e64 s[34:35], 0, v53
	v_cmp_lt_i32_e64 s[36:37], 1, v53
	v_cmp_lt_i32_e64 s[38:39], 2, v53
	v_cmp_lt_i32_e64 s[40:41], 3, v53
	v_cndmask_b32_e64 v36, v70, v36, s[34:35]
	v_cndmask_b32_e64 v38, v70, v38, s[36:37]
	v_cndmask_b32_e64 v42, v70, v42, s[38:39]
	v_cndmask_b32_e64 v46, v70, v46, s[40:41]
	v_cvt_f32_f16_e32 v62, v64
	v_cndmask_b32_e32 v34, v34, v39, vcc
	v_lshlrev_b32_e32 v85, 2, v34
	s_waitcnt lgkmcnt(0)
	v_max_i32_e32 v34, v53, v35
	ds_bpermute_b32 v35, v85, v34
	v_cvt_f32_f16_sdwa v63, v64 dst_sel:DWORD dst_unused:UNUSED_PAD src0_sel:WORD_1
	v_cvt_f32_f16_e32 v60, v65
	v_cvt_f32_f16_sdwa v61, v65 dst_sel:DWORD dst_unused:UNUSED_PAD src0_sel:WORD_1
	v_cvt_f32_f16_e32 v58, v66
	v_cvt_f32_f16_sdwa v59, v66 dst_sel:DWORD dst_unused:UNUSED_PAD src0_sel:WORD_1
	v_cvt_f32_f16_e32 v56, v67
	v_cvt_f32_f16_sdwa v57, v67 dst_sel:DWORD dst_unused:UNUSED_PAD src0_sel:WORD_1
	s_waitcnt lgkmcnt(0)
	v_max_i32_e32 v34, v34, v35
	s_nop 0
	v_readfirstlane_b32 s31, v34
	s_cmp_lt_i32 s31, 1
	s_cbranch_scc1 .LBB2_19
